# FoX tile-skip bound: max of the q gain squared computed lane-parallel (2 loads per lane + the existing wave max) instead of a 64-iteration serial load loop in the 8 prefix workgroups
# speedup vs baseline: 1.0033x; 1.0033x over previous
; #define LAS __attribute__((address_space(3)))
; __global__ void __launch_bounds__(NTHREADS, 2) mega_fwd(Args args) {
;     ...
;             const double base = sd[tid];
; #pragma unroll
;             for (int i = 0; i < 16; ++i) CC[(size_t)h * S + tid * 16 + i] = (float)(base + loc[i]);
;             LAS float* cend = (LAS float*)(F.lds + 8192); LAS float* cp0 = cend + 128; LAS float* redm = cp0 + 32;
;             { float mq = 0.f, mk = 0.f;
;               { const float* gq = args.in[6]; for (int i = 0; i < HD; ++i) mq = fmaxf(mq, gq[i] * gq[i]); mq *= (float)HD; }
.LBB0_623:
	s_or_b64 exec, exec, s[0:1]
	s_ashr_i32 s7, s6, 31
	s_waitcnt lgkmcnt(0)
	s_barrier
	ds_read_b64 v[54:55], v38
	s_lshl_b64 s[8:9], s[6:7], 15
	v_readlane_b32 s0, v241, 5
	v_readlane_b32 s1, v241, 6
	s_add_u32 s0, s0, s8
	s_addc_u32 s1, s1, s9
	v_lshlrev_b32_e32 v52, 2, v1
	v_mov_b32_e32 v53, 0
	v_lshl_add_u64 v[38:39], s[0:1], 0, v[52:53]
	s_mov_b64 s[0:1], 0x1c0000
	v_lshl_add_u64 v[56:57], v[38:39], 0, s[0:1]
	s_mov_b32 s0, 0x1c0000
	s_waitcnt lgkmcnt(0)
	v_add_f64 v[46:47], v[54:55], v[30:31]
	v_add_co_u32_e32 v30, vcc, s0, v38
	v_add_f64 v[48:49], v[54:55], v[36:37]
	v_add_f64 v[50:51], v[54:55], v[34:35]
	v_add_f64 v[44:45], v[54:55], v[32:33]
	v_addc_co_u32_e32 v31, vcc, 0, v39, vcc
	v_add_f64 v[40:41], v[54:55], v[28:29]
	v_add_f64 v[42:43], v[54:55], v[26:27]
	v_add_f64 v[36:37], v[54:55], v[24:25]
	v_add_f64 v[38:39], v[54:55], v[22:23]
	v_cvt_f32_f64_e32 v3, v[48:49]
	v_cvt_f32_f64_e32 v2, v[50:51]
	v_cvt_f32_f64_e32 v5, v[44:45]
	v_cvt_f32_f64_e32 v4, v[46:47]
	v_cvt_f32_f64_e32 v27, v[40:41]
	v_cvt_f32_f64_e32 v26, v[42:43]
	v_cvt_f32_f64_e32 v29, v[36:37]
	v_cvt_f32_f64_e32 v28, v[38:39]
	global_store_dwordx4 v[30:31], v[2:5], off
	global_store_dwordx4 v[56:57], v[26:29], off offset:16
	v_add_f64 v[32:33], v[54:55], v[20:21]
	v_add_f64 v[34:35], v[54:55], v[18:19]
	v_add_f64 v[28:29], v[54:55], v[16:17]
	v_add_f64 v[30:31], v[54:55], v[14:15]
	v_cvt_f32_f64_e32 v19, v[32:33]
	v_cvt_f32_f64_e32 v18, v[34:35]
	v_cvt_f32_f64_e32 v21, v[28:29]
	v_cvt_f32_f64_e32 v20, v[30:31]
	global_store_dwordx4 v[56:57], v[18:21], off offset:32
	v_add_f64 v[24:25], v[54:55], v[12:13]
	v_add_f64 v[26:27], v[54:55], v[10:11]
	v_add_f64 v[20:21], v[54:55], v[8:9]
	v_add_f64 v[22:23], v[54:55], v[6:7]
	v_cvt_f32_f64_e32 v5, v[24:25]
	v_cvt_f32_f64_e32 v4, v[26:27]
	v_cvt_f32_f64_e32 v7, v[20:21]
	v_cvt_f32_f64_e32 v6, v[22:23]
	global_store_dwordx4 v[56:57], v[4:7], off offset:48
	v_mbcnt_lo_u32_b32 v3, -1, 0
	v_mbcnt_hi_u32_b32 v3, -1, v3
	v_lshlrev_b32_e32 v3, 2, v3
	global_load_dword v4, v3, s[88:89]
	global_load_dword v5, v3, s[88:89] offset:256
	s_waitcnt vmcnt(0)
	v_mul_f32_e32 v4, v4, v4
	v_mul_f32_e32 v5, v5, v5
	v_max_f32_e32 v6, v4, v5
